# alignment pads: 4 bytes before P5 loop, 4 before P8 loop, 12 before P9 loop so that fewer 8-byte instructions straddle 32/64-byte fetch lines in those K-loops
# baseline (speedup 1.0000x reference)
.LBB0_940:
	s_nop 0
	v_readlane_b32 s2, v251, 14
	v_readlane_b32 s3, v251, 15
	s_cmp_lt_i32 s2, 6
	s_cselect_b64 s[2:3], -1, 0
	s_and_b64 s[0:1], s[2:3], s[0:1]
	s_andn2_b64 vcc, exec, s[0:1]
	s_cbranch_vccnz .LBB0_965
	v_readlane_b32 s0, v251, 0
	s_cmpk_gt_i32 s0, 0x1ff
	v_mbcnt_lo_u32_b32 v0, -1, 0
	v_mbcnt_hi_u32_b32 v0, -1, v0
	v_readlane_b32 s1, v251, 1
	v_mbcnt_lo_u32_b32 v8, -1, 0
	v_mbcnt_hi_u32_b32 v8, -1, v8
	s_cbranch_scc1 .LBB0_965
	v_readlane_b32 s0, v251, 0
	s_waitcnt lgkmcnt(0)
	s_ashr_i32 s15, s0, 31
	s_mov_b32 s4, s0
	s_lshr_b32 s0, s15, 29
	s_add_i32 s5, s4, s0
	s_and_b32 s0, s5, -8
	s_sub_i32 s6, s4, s0
	s_cmp_gt_i32 s6, -1
	v_readlane_b32 s1, v251, 1
	s_cbranch_scc0 .LBB0_944
	s_lshl_b32 s4, s6, 6
	s_cbranch_execz .LBB0_945
	s_branch .LBB0_946

.LBB0_1167:
	s_nop 0
	v_readlane_b32 s2, v251, 14
	v_readlane_b32 s3, v251, 15
	s_cmp_lt_i32 s2, 9
	s_cselect_b64 s[2:3], -1, 0
	s_and_b64 s[0:1], s[2:3], s[0:1]
	s_andn2_b64 vcc, exec, s[0:1]
	s_cbranch_vccnz .LBB0_1200
	v_readlane_b32 s0, v251, 16
	v_mbcnt_lo_u32_b32 v0, -1, 0
	v_mbcnt_hi_u32_b32 v0, -1, v0
	s_andn2_b32 s0, s0, 63
	s_nop 0
	v_add_u32_e32 v0, s0, v0
	v_cmp_gt_i32_e32 vcc, 33, v0
	s_waitcnt lgkmcnt(0)
	v_lshl_add_u32 v2, v0, 2, 0
	s_and_saveexec_b64 s[4:5], vcc
	s_cbranch_execz .LBB0_1170
	v_readlane_b32 s8, v251, 10
	v_ashrrev_i32_e32 v1, 31, v0
	v_readlane_b32 s10, v251, 12
	v_readlane_b32 s11, v251, 13
	v_add_u32_e32 v3, 0x24240, v2
	v_readlane_b32 s9, v251, 11
	v_lshl_add_u64 v[4:5], v[0:1], 2, s[10:11]
	v_add_co_u32_e32 v4, vcc, 0x66280000, v4
	s_nop 1
	v_addc_co_u32_e32 v5, vcc, 0, v5, vcc
	global_load_dword v1, v[4:5], off
	s_waitcnt vmcnt(0)
	ds_write_b32 v3, v1

.LBB0_1252:
	s_nop 0
	s_nop 0
	s_nop 0
	v_readlane_b32 s2, v251, 14
	v_readlane_b32 s3, v251, 15
	s_cmp_lt_i32 s2, 10
	s_cselect_b64 s[2:3], -1, 0
	s_and_b64 s[0:1], s[2:3], s[0:1]
	s_andn2_b64 vcc, exec, s[0:1]
	s_cbranch_vccnz .LBB0_1293
	v_readlane_b32 s0, v251, 16
	v_mbcnt_lo_u32_b32 v0, -1, 0
	v_mbcnt_hi_u32_b32 v0, -1, v0
	s_and_b32 s6, s0, 0xffffffc0
	v_add_u32_e32 v0, s6, v0
	v_cmp_gt_i32_e32 vcc, 33, v0
	s_waitcnt lgkmcnt(0)
	v_lshl_add_u32 v2, v0, 2, 0
	s_and_saveexec_b64 s[0:1], vcc
	s_cbranch_execz .LBB0_1255
	v_readlane_b32 s8, v251, 10
	v_ashrrev_i32_e32 v1, 31, v0
	v_readlane_b32 s10, v251, 12
	v_readlane_b32 s11, v251, 13
	v_add_u32_e32 v3, 0x24240, v2
	v_readlane_b32 s9, v251, 11
	v_lshl_add_u64 v[4:5], v[0:1], 2, s[10:11]
	v_add_co_u32_e32 v4, vcc, 0x66280000, v4
	s_nop 1
	v_addc_co_u32_e32 v5, vcc, 0, v5, vcc
	global_load_dword v1, v[4:5], off
	s_waitcnt vmcnt(0)
	ds_write_b32 v3, v1
